# v23 + code placement: the seven GEMM K-loop heads aligned to 64 bytes (.p2align 6, s_nop padding outside the loops)
# baseline (speedup 1.0000x reference)
.LBB0_170:
	s_ashr_i32 s55, s54, 31
	s_lshl_b64 s[56:57], s[54:55], 20
	s_add_u32 s56, s12, s56
	s_addc_u32 s57, s13, s57
	s_and_b64 s[58:59], s[42:43], exec
	s_cselect_b32 s15, s57, s63
	s_cselect_b32 s29, s56, s62
	s_ashr_i32 s53, s52, 31
	s_lshl_b64 s[58:59], s[52:53], 20
	s_add_u32 s58, s20, s58
	s_addc_u32 s59, s21, s59
	s_and_b64 s[66:67], s[42:43], exec
	s_cselect_b32 s53, s59, s65
	s_cselect_b32 s55, s58, s64
	s_add_u32 s62, s62, 0xc000
	s_addc_u32 s63, s63, 0
	s_add_u32 s61, s64, 0x10000
	v_mov_b32_e32 v2, 0
	s_addc_u32 vcc_lo, s65, 0
	s_mov_b32 vcc_hi, -2
	v_mov_b32_e32 v3, v2
	v_mov_b32_e32 v4, v2
	v_mov_b32_e32 v5, v2
	s_waitcnt lgkmcnt(0)
	v_mov_b32_e32 v6, v2
	v_mov_b32_e32 v7, v2
	v_mov_b32_e32 v8, v2
	v_mov_b32_e32 v9, v2
	v_mov_b32_e32 v18, v2
	v_mov_b32_e32 v19, v2
	v_mov_b32_e32 v20, v2
	v_mov_b32_e32 v21, v2
	v_mov_b32_e32 v22, v2
	v_mov_b32_e32 v23, v2
	v_mov_b32_e32 v24, v2
	v_mov_b32_e32 v25, v2
	v_mov_b32_e32 v34, v2
	v_mov_b32_e32 v35, v2
	v_mov_b32_e32 v36, v2
	v_mov_b32_e32 v37, v2
	v_mov_b32_e32 v38, v2
	v_mov_b32_e32 v39, v2
	v_mov_b32_e32 v40, v2
	v_mov_b32_e32 v41, v2
	v_mov_b32_e32 v50, v2
	v_mov_b32_e32 v51, v2
	v_mov_b32_e32 v52, v2
	v_mov_b32_e32 v53, v2
	v_mov_b32_e32 v54, v2
	v_mov_b32_e32 v55, v2
	v_mov_b32_e32 v56, v2
	v_mov_b32_e32 v57, v2
	v_mov_b32_e32 v10, v2
	v_mov_b32_e32 v11, v2
	v_mov_b32_e32 v12, v2
	v_mov_b32_e32 v13, v2
	v_mov_b32_e32 v14, v2
	v_mov_b32_e32 v15, v2
	v_mov_b32_e32 v16, v2
	v_mov_b32_e32 v17, v2
	v_mov_b32_e32 v26, v2
	v_mov_b32_e32 v27, v2
	v_mov_b32_e32 v28, v2
	v_mov_b32_e32 v29, v2
	v_mov_b32_e32 v30, v2
	v_mov_b32_e32 v31, v2
	v_mov_b32_e32 v32, v2
	v_mov_b32_e32 v33, v2
	v_mov_b32_e32 v42, v2
	v_mov_b32_e32 v43, v2
	v_mov_b32_e32 v44, v2
	v_mov_b32_e32 v45, v2
	v_mov_b32_e32 v46, v2
	v_mov_b32_e32 v47, v2
	v_mov_b32_e32 v48, v2
	v_mov_b32_e32 v49, v2
	v_mov_b32_e32 v58, v2
	v_mov_b32_e32 v59, v2
	v_mov_b32_e32 v60, v2
	v_mov_b32_e32 v61, v2
	v_mov_b32_e32 v62, v2
	v_mov_b32_e32 v63, v2
	v_mov_b32_e32 v64, v2
	v_mov_b32_e32 v65, v2
	v_mov_b32_e32 v66, v2
	v_mov_b32_e32 v67, v2
	v_mov_b32_e32 v68, v2
	v_mov_b32_e32 v69, v2
	v_mov_b32_e32 v70, v2
	v_mov_b32_e32 v71, v2
	v_mov_b32_e32 v72, v2
	v_mov_b32_e32 v73, v2
	v_mov_b32_e32 v98, v2
	v_mov_b32_e32 v99, v2
	v_mov_b32_e32 v100, v2
	v_mov_b32_e32 v101, v2
	v_mov_b32_e32 v102, v2
	v_mov_b32_e32 v103, v2
	v_mov_b32_e32 v104, v2
	v_mov_b32_e32 v105, v2
	v_mov_b32_e32 v116, v2
	v_mov_b32_e32 v117, v2
	v_mov_b32_e32 v118, v2
	v_mov_b32_e32 v119, v2
	v_mov_b32_e32 v120, v2
	v_mov_b32_e32 v121, v2
	v_mov_b32_e32 v122, v2
	v_mov_b32_e32 v123, v2
	v_mov_b32_e32 v132, v2
	v_mov_b32_e32 v133, v2
	v_mov_b32_e32 v134, v2
	v_mov_b32_e32 v135, v2
	v_mov_b32_e32 v136, v2
	v_mov_b32_e32 v137, v2
	v_mov_b32_e32 v138, v2
	v_mov_b32_e32 v139, v2
	v_mov_b32_e32 v74, v2
	v_mov_b32_e32 v75, v2
	v_mov_b32_e32 v76, v2
	v_mov_b32_e32 v77, v2
	v_mov_b32_e32 v78, v2
	v_mov_b32_e32 v79, v2
	v_mov_b32_e32 v80, v2
	v_mov_b32_e32 v81, v2
	v_mov_b32_e32 v106, v2
	v_mov_b32_e32 v107, v2
	v_mov_b32_e32 v108, v2
	v_mov_b32_e32 v109, v2
	v_mov_b32_e32 v110, v2
	v_mov_b32_e32 v111, v2
	v_mov_b32_e32 v112, v2
	v_mov_b32_e32 v113, v2
	v_mov_b32_e32 v124, v2
	v_mov_b32_e32 v125, v2
	v_mov_b32_e32 v126, v2
	v_mov_b32_e32 v127, v2
	v_mov_b32_e32 v128, v2
	v_mov_b32_e32 v129, v2
	v_mov_b32_e32 v130, v2
	v_mov_b32_e32 v131, v2
	v_mov_b32_e32 v140, v2
	v_mov_b32_e32 v141, v2
	v_mov_b32_e32 v142, v2
	v_mov_b32_e32 v143, v2
	v_mov_b32_e32 v144, v2
	v_mov_b32_e32 v145, v2
	v_mov_b32_e32 v146, v2
	v_mov_b32_e32 v147, v2
	.p2align	6

.LBB0_345:
	s_ashr_i32 s51, s50, 31
	s_lshl_b64 s[52:53], s[50:51], 20
	s_add_u32 s52, s5, s52
	s_addc_u32 s53, s8, s53
	s_and_b64 s[54:55], s[38:39], exec
	s_cselect_b32 s15, s53, s57
	s_cselect_b32 s29, s52, s56
	s_ashr_i32 s49, s48, 31
	s_lshl_b64 s[54:55], s[48:49], 20
	s_add_u32 s54, s9, s54
	s_addc_u32 s55, s12, s55
	s_and_b64 s[60:61], s[38:39], exec
	s_cselect_b32 s41, s55, s59
	s_cselect_b32 s49, s54, s58
	s_add_u32 s56, s56, 0xc000
	s_addc_u32 s57, s57, 0
	s_add_u32 s51, s58, 0x10000
	v_mov_b32_e32 v2, 0
	s_addc_u32 s69, s59, 0
	s_mov_b32 s70, -2
	v_mov_b32_e32 v3, v2
	v_mov_b32_e32 v4, v2
	v_mov_b32_e32 v5, v2
	v_mov_b32_e32 v6, v2
	v_mov_b32_e32 v7, v2
	v_mov_b32_e32 v8, v2
	v_mov_b32_e32 v9, v2
	v_mov_b32_e32 v18, v2
	v_mov_b32_e32 v19, v2
	v_mov_b32_e32 v20, v2
	v_mov_b32_e32 v21, v2
	v_mov_b32_e32 v22, v2
	v_mov_b32_e32 v23, v2
	v_mov_b32_e32 v24, v2
	v_mov_b32_e32 v25, v2
	v_mov_b32_e32 v34, v2
	v_mov_b32_e32 v35, v2
	v_mov_b32_e32 v36, v2
	v_mov_b32_e32 v37, v2
	v_mov_b32_e32 v38, v2
	v_mov_b32_e32 v39, v2
	v_mov_b32_e32 v40, v2
	v_mov_b32_e32 v41, v2
	v_mov_b32_e32 v50, v2
	v_mov_b32_e32 v51, v2
	v_mov_b32_e32 v52, v2
	v_mov_b32_e32 v53, v2
	v_mov_b32_e32 v54, v2
	v_mov_b32_e32 v55, v2
	v_mov_b32_e32 v56, v2
	v_mov_b32_e32 v57, v2
	v_mov_b32_e32 v10, v2
	v_mov_b32_e32 v11, v2
	v_mov_b32_e32 v12, v2
	v_mov_b32_e32 v13, v2
	v_mov_b32_e32 v14, v2
	v_mov_b32_e32 v15, v2
	v_mov_b32_e32 v16, v2
	v_mov_b32_e32 v17, v2
	v_mov_b32_e32 v26, v2
	v_mov_b32_e32 v27, v2
	v_mov_b32_e32 v28, v2
	v_mov_b32_e32 v29, v2
	v_mov_b32_e32 v30, v2
	v_mov_b32_e32 v31, v2
	v_mov_b32_e32 v32, v2
	v_mov_b32_e32 v33, v2
	v_mov_b32_e32 v42, v2
	v_mov_b32_e32 v43, v2
	v_mov_b32_e32 v44, v2
	v_mov_b32_e32 v45, v2
	v_mov_b32_e32 v46, v2
	v_mov_b32_e32 v47, v2
	v_mov_b32_e32 v48, v2
	v_mov_b32_e32 v49, v2
	v_mov_b32_e32 v58, v2
	v_mov_b32_e32 v59, v2
	v_mov_b32_e32 v60, v2
	v_mov_b32_e32 v61, v2
	v_mov_b32_e32 v62, v2
	v_mov_b32_e32 v63, v2
	v_mov_b32_e32 v64, v2
	v_mov_b32_e32 v65, v2
	v_mov_b32_e32 v66, v2
	v_mov_b32_e32 v67, v2
	v_mov_b32_e32 v68, v2
	v_mov_b32_e32 v69, v2
	v_mov_b32_e32 v70, v2
	v_mov_b32_e32 v71, v2
	v_mov_b32_e32 v72, v2
	v_mov_b32_e32 v73, v2
	v_mov_b32_e32 v82, v2
	v_mov_b32_e32 v83, v2
	v_mov_b32_e32 v84, v2
	v_mov_b32_e32 v85, v2
	v_mov_b32_e32 v86, v2
	v_mov_b32_e32 v87, v2
	v_mov_b32_e32 v88, v2
	v_mov_b32_e32 v89, v2
	v_mov_b32_e32 v98, v2
	v_mov_b32_e32 v99, v2
	v_mov_b32_e32 v100, v2
	v_mov_b32_e32 v101, v2
	v_mov_b32_e32 v102, v2
	v_mov_b32_e32 v103, v2
	v_mov_b32_e32 v104, v2
	v_mov_b32_e32 v105, v2
	v_mov_b32_e32 v116, v2
	v_mov_b32_e32 v117, v2
	v_mov_b32_e32 v118, v2
	v_mov_b32_e32 v119, v2
	v_mov_b32_e32 v120, v2
	v_mov_b32_e32 v121, v2
	v_mov_b32_e32 v122, v2
	v_mov_b32_e32 v123, v2
	v_mov_b32_e32 v74, v2
	v_mov_b32_e32 v75, v2
	v_mov_b32_e32 v76, v2
	v_mov_b32_e32 v77, v2
	v_mov_b32_e32 v78, v2
	v_mov_b32_e32 v79, v2
	v_mov_b32_e32 v80, v2
	v_mov_b32_e32 v81, v2
	v_mov_b32_e32 v90, v2
	v_mov_b32_e32 v91, v2
	v_mov_b32_e32 v92, v2
	v_mov_b32_e32 v93, v2
	v_mov_b32_e32 v94, v2
	v_mov_b32_e32 v95, v2
	v_mov_b32_e32 v96, v2
	v_mov_b32_e32 v97, v2
	v_mov_b32_e32 v106, v2
	v_mov_b32_e32 v107, v2
	v_mov_b32_e32 v108, v2
	v_mov_b32_e32 v109, v2
	v_mov_b32_e32 v110, v2
	v_mov_b32_e32 v111, v2
	v_mov_b32_e32 v112, v2
	v_mov_b32_e32 v113, v2
	v_mov_b32_e32 v124, v2
	v_mov_b32_e32 v125, v2
	v_mov_b32_e32 v126, v2
	v_mov_b32_e32 v127, v2
	v_mov_b32_e32 v128, v2
	v_mov_b32_e32 v129, v2
	v_mov_b32_e32 v130, v2
	v_mov_b32_e32 v131, v2
	.p2align	6

.LBB0_502:
	s_ashr_i32 s49, s48, 31
	s_lshl_b64 s[50:51], s[48:49], 20
	s_add_u32 s50, s5, s50
	s_addc_u32 s51, s7, s51
	s_and_b64 s[52:53], s[38:39], exec
	s_cselect_b32 s15, s51, s55
	s_cselect_b32 s29, s50, s54
	s_ashr_i32 s47, s46, 31
	s_lshl_b64 s[52:53], s[46:47], 20
	s_add_u32 s52, s8, s52
	s_addc_u32 s53, s9, s53
	s_and_b64 s[58:59], s[38:39], exec
	s_cselect_b32 s41, s53, s57
	s_cselect_b32 s47, s52, s56
	s_add_u32 s54, s54, 0xc000
	s_addc_u32 s55, s55, 0
	s_add_u32 s49, s56, 0x10000
	v_mov_b32_e32 v2, 0
	s_addc_u32 s66, s57, 0
	s_mov_b32 s67, -2
	v_mov_b32_e32 v3, v2
	v_mov_b32_e32 v4, v2
	v_mov_b32_e32 v5, v2
	v_mov_b32_e32 v6, v2
	v_mov_b32_e32 v7, v2
	v_mov_b32_e32 v8, v2
	v_mov_b32_e32 v9, v2
	v_mov_b32_e32 v18, v2
	v_mov_b32_e32 v19, v2
	v_mov_b32_e32 v20, v2
	v_mov_b32_e32 v21, v2
	v_mov_b32_e32 v22, v2
	v_mov_b32_e32 v23, v2
	v_mov_b32_e32 v24, v2
	v_mov_b32_e32 v25, v2
	v_mov_b32_e32 v34, v2
	v_mov_b32_e32 v35, v2
	v_mov_b32_e32 v36, v2
	v_mov_b32_e32 v37, v2
	v_mov_b32_e32 v38, v2
	v_mov_b32_e32 v39, v2
	v_mov_b32_e32 v40, v2
	v_mov_b32_e32 v41, v2
	v_mov_b32_e32 v50, v2
	v_mov_b32_e32 v51, v2
	v_mov_b32_e32 v52, v2
	v_mov_b32_e32 v53, v2
	v_mov_b32_e32 v54, v2
	v_mov_b32_e32 v55, v2
	v_mov_b32_e32 v56, v2
	v_mov_b32_e32 v57, v2
	v_mov_b32_e32 v10, v2
	v_mov_b32_e32 v11, v2
	v_mov_b32_e32 v12, v2
	v_mov_b32_e32 v13, v2
	v_mov_b32_e32 v14, v2
	v_mov_b32_e32 v15, v2
	v_mov_b32_e32 v16, v2
	v_mov_b32_e32 v17, v2
	v_mov_b32_e32 v26, v2
	v_mov_b32_e32 v27, v2
	v_mov_b32_e32 v28, v2
	v_mov_b32_e32 v29, v2
	v_mov_b32_e32 v30, v2
	v_mov_b32_e32 v31, v2
	v_mov_b32_e32 v32, v2
	v_mov_b32_e32 v33, v2
	v_mov_b32_e32 v42, v2
	v_mov_b32_e32 v43, v2
	v_mov_b32_e32 v44, v2
	v_mov_b32_e32 v45, v2
	v_mov_b32_e32 v46, v2
	v_mov_b32_e32 v47, v2
	v_mov_b32_e32 v48, v2
	v_mov_b32_e32 v49, v2
	v_mov_b32_e32 v58, v2
	v_mov_b32_e32 v59, v2
	v_mov_b32_e32 v60, v2
	v_mov_b32_e32 v61, v2
	v_mov_b32_e32 v62, v2
	v_mov_b32_e32 v63, v2
	v_mov_b32_e32 v64, v2
	v_mov_b32_e32 v65, v2
	v_mov_b32_e32 v66, v2
	v_mov_b32_e32 v67, v2
	v_mov_b32_e32 v68, v2
	v_mov_b32_e32 v69, v2
	v_mov_b32_e32 v70, v2
	v_mov_b32_e32 v71, v2
	v_mov_b32_e32 v72, v2
	v_mov_b32_e32 v73, v2
	v_mov_b32_e32 v82, v2
	v_mov_b32_e32 v83, v2
	v_mov_b32_e32 v84, v2
	v_mov_b32_e32 v85, v2
	v_mov_b32_e32 v86, v2
	v_mov_b32_e32 v87, v2
	v_mov_b32_e32 v88, v2
	v_mov_b32_e32 v89, v2
	v_mov_b32_e32 v98, v2
	v_mov_b32_e32 v99, v2
	v_mov_b32_e32 v100, v2
	v_mov_b32_e32 v101, v2
	v_mov_b32_e32 v102, v2
	v_mov_b32_e32 v103, v2
	v_mov_b32_e32 v104, v2
	v_mov_b32_e32 v105, v2
	v_mov_b32_e32 v116, v2
	v_mov_b32_e32 v117, v2
	v_mov_b32_e32 v118, v2
	v_mov_b32_e32 v119, v2
	v_mov_b32_e32 v120, v2
	v_mov_b32_e32 v121, v2
	v_mov_b32_e32 v122, v2
	v_mov_b32_e32 v123, v2
	v_mov_b32_e32 v74, v2
	v_mov_b32_e32 v75, v2
	v_mov_b32_e32 v76, v2
	v_mov_b32_e32 v77, v2
	v_mov_b32_e32 v78, v2
	v_mov_b32_e32 v79, v2
	v_mov_b32_e32 v80, v2
	v_mov_b32_e32 v81, v2
	v_mov_b32_e32 v90, v2
	v_mov_b32_e32 v91, v2
	v_mov_b32_e32 v92, v2
	v_mov_b32_e32 v93, v2
	v_mov_b32_e32 v94, v2
	v_mov_b32_e32 v95, v2
	v_mov_b32_e32 v96, v2
	v_mov_b32_e32 v97, v2
	v_mov_b32_e32 v106, v2
	v_mov_b32_e32 v107, v2
	v_mov_b32_e32 v108, v2
	v_mov_b32_e32 v109, v2
	v_mov_b32_e32 v110, v2
	v_mov_b32_e32 v111, v2
	v_mov_b32_e32 v112, v2
	v_mov_b32_e32 v113, v2
	v_mov_b32_e32 v124, v2
	v_mov_b32_e32 v125, v2
	v_mov_b32_e32 v126, v2
	v_mov_b32_e32 v127, v2
	v_mov_b32_e32 v128, v2
	v_mov_b32_e32 v129, v2
	v_mov_b32_e32 v130, v2
	v_mov_b32_e32 v131, v2
	.p2align	6

.LBB0_1078:
	s_ashr_i32 s29, s28, 31
	s_lshl_b64 s[16:17], s[28:29], 20
	s_add_u32 s42, s14, s16
	s_addc_u32 s43, s15, s17
	s_and_b64 s[16:17], s[40:41], exec
	s_cselect_b32 s24, s43, s53
	s_cselect_b32 s29, s42, s52
	s_ashr_i32 s27, s26, 31
	s_lshl_b64 s[16:17], s[26:27], 20
	s_add_u32 s44, s0, s16
	s_addc_u32 s45, s1, s17
	s_and_b64 s[16:17], s[40:41], exec
	s_cselect_b32 s27, s45, s51
	s_cselect_b32 s47, s44, s50
	s_add_u32 s52, s52, 0xc000
	s_addc_u32 s53, s53, 0
	s_add_u32 s49, s50, 0x10000
	s_addc_u32 s63, s51, 0
	s_mov_b32 s64, -2
	.p2align	6

.LBB0_1229:
	s_ashr_i32 s29, s28, 31
	s_lshl_b64 s[16:17], s[28:29], 20
	s_add_u32 s40, s12, s16
	s_addc_u32 s41, s13, s17
	s_and_b64 s[16:17], s[38:39], exec
	s_cselect_b32 s29, s41, s47
	s_cselect_b32 s60, s40, s46
	s_ashr_i32 s27, s26, 31
	s_lshl_b64 s[16:17], s[26:27], 20
	s_add_u32 s42, s14, s16
	s_addc_u32 s43, s15, s17
	s_and_b64 s[16:17], s[38:39], exec
	s_cselect_b32 s27, s43, s49
	s_cselect_b32 s61, s42, s48
	s_add_u32 s46, s46, 0xc000
	s_addc_u32 s47, s47, 0
	s_add_u32 s62, s48, 0x10000
	v_mov_b32_e32 v2, 0
	s_addc_u32 s63, s49, 0
	s_mov_b32 s64, -2
	v_mov_b32_e32 v3, v2
	v_mov_b32_e32 v4, v2
	v_mov_b32_e32 v5, v2
	v_mov_b32_e32 v6, v2
	v_mov_b32_e32 v7, v2
	v_mov_b32_e32 v8, v2
	v_mov_b32_e32 v9, v2
	v_mov_b32_e32 v18, v2
	v_mov_b32_e32 v19, v2
	v_mov_b32_e32 v20, v2
	v_mov_b32_e32 v21, v2
	v_mov_b32_e32 v22, v2
	v_mov_b32_e32 v23, v2
	v_mov_b32_e32 v24, v2
	v_mov_b32_e32 v25, v2
	v_mov_b32_e32 v34, v2
	v_mov_b32_e32 v35, v2
	v_mov_b32_e32 v36, v2
	v_mov_b32_e32 v37, v2
	v_mov_b32_e32 v38, v2
	v_mov_b32_e32 v39, v2
	v_mov_b32_e32 v40, v2
	v_mov_b32_e32 v41, v2
	v_mov_b32_e32 v50, v2
	v_mov_b32_e32 v51, v2
	v_mov_b32_e32 v52, v2
	v_mov_b32_e32 v53, v2
	v_mov_b32_e32 v54, v2
	v_mov_b32_e32 v55, v2
	v_mov_b32_e32 v56, v2
	v_mov_b32_e32 v57, v2
	v_mov_b32_e32 v10, v2
	v_mov_b32_e32 v11, v2
	v_mov_b32_e32 v12, v2
	v_mov_b32_e32 v13, v2
	v_mov_b32_e32 v14, v2
	v_mov_b32_e32 v15, v2
	v_mov_b32_e32 v16, v2
	v_mov_b32_e32 v17, v2
	v_mov_b32_e32 v26, v2
	v_mov_b32_e32 v27, v2
	v_mov_b32_e32 v28, v2
	v_mov_b32_e32 v29, v2
	v_mov_b32_e32 v30, v2
	v_mov_b32_e32 v31, v2
	v_mov_b32_e32 v32, v2
	v_mov_b32_e32 v33, v2
	v_mov_b32_e32 v42, v2
	v_mov_b32_e32 v43, v2
	v_mov_b32_e32 v44, v2
	v_mov_b32_e32 v45, v2
	v_mov_b32_e32 v46, v2
	v_mov_b32_e32 v47, v2
	v_mov_b32_e32 v48, v2
	v_mov_b32_e32 v49, v2
	v_mov_b32_e32 v58, v2
	v_mov_b32_e32 v59, v2
	v_mov_b32_e32 v60, v2
	v_mov_b32_e32 v61, v2
	v_mov_b32_e32 v62, v2
	v_mov_b32_e32 v63, v2
	v_mov_b32_e32 v64, v2
	v_mov_b32_e32 v65, v2
	v_mov_b32_e32 v66, v2
	v_mov_b32_e32 v67, v2
	v_mov_b32_e32 v68, v2
	v_mov_b32_e32 v69, v2
	v_mov_b32_e32 v70, v2
	v_mov_b32_e32 v71, v2
	v_mov_b32_e32 v72, v2
	v_mov_b32_e32 v73, v2
	v_mov_b32_e32 v82, v2
	v_mov_b32_e32 v83, v2
	v_mov_b32_e32 v84, v2
	v_mov_b32_e32 v85, v2
	v_mov_b32_e32 v86, v2
	v_mov_b32_e32 v87, v2
	v_mov_b32_e32 v88, v2
	v_mov_b32_e32 v89, v2
	v_mov_b32_e32 v98, v2
	v_mov_b32_e32 v99, v2
	v_mov_b32_e32 v100, v2
	v_mov_b32_e32 v101, v2
	v_mov_b32_e32 v102, v2
	v_mov_b32_e32 v103, v2
	v_mov_b32_e32 v104, v2
	v_mov_b32_e32 v105, v2
	v_mov_b32_e32 v116, v2
	v_mov_b32_e32 v117, v2
	v_mov_b32_e32 v118, v2
	v_mov_b32_e32 v119, v2
	v_mov_b32_e32 v120, v2
	v_mov_b32_e32 v121, v2
	v_mov_b32_e32 v122, v2
	v_mov_b32_e32 v123, v2
	v_mov_b32_e32 v74, v2
	v_mov_b32_e32 v75, v2
	v_mov_b32_e32 v76, v2
	v_mov_b32_e32 v77, v2
	v_mov_b32_e32 v78, v2
	v_mov_b32_e32 v79, v2
	v_mov_b32_e32 v80, v2
	v_mov_b32_e32 v81, v2
	v_mov_b32_e32 v90, v2
	v_mov_b32_e32 v91, v2
	v_mov_b32_e32 v92, v2
	v_mov_b32_e32 v93, v2
	v_mov_b32_e32 v94, v2
	v_mov_b32_e32 v95, v2
	v_mov_b32_e32 v96, v2
	v_mov_b32_e32 v97, v2
	v_mov_b32_e32 v106, v2
	v_mov_b32_e32 v107, v2
	v_mov_b32_e32 v108, v2
	v_mov_b32_e32 v109, v2
	v_mov_b32_e32 v110, v2
	v_mov_b32_e32 v111, v2
	v_mov_b32_e32 v112, v2
	v_mov_b32_e32 v113, v2
	v_mov_b32_e32 v124, v2
	v_mov_b32_e32 v125, v2
	v_mov_b32_e32 v126, v2
	v_mov_b32_e32 v127, v2
	v_mov_b32_e32 v128, v2
	v_mov_b32_e32 v129, v2
	v_mov_b32_e32 v130, v2
	v_mov_b32_e32 v131, v2
	.p2align	6

.LBB0_1333:
	s_ashr_i32 s29, s28, 31
	s_lshl_b64 s[16:17], s[28:29], 22
	s_add_u32 s42, s12, s16
	s_addc_u32 s43, s13, s17
	s_and_b64 s[16:17], s[40:41], exec
	s_cselect_b32 s24, s43, s53
	s_cselect_b32 s29, s42, s52
	s_ashr_i32 s27, s26, 31
	s_lshl_b64 s[16:17], s[26:27], 22
	s_add_u32 s44, s20, s16
	s_addc_u32 s45, s21, s17
	s_and_b64 s[16:17], s[40:41], exec
	s_cselect_b32 s27, s45, s51
	s_cselect_b32 s47, s44, s50
	s_add_u32 s52, s52, 0xc000
	s_addc_u32 s53, s53, 0
	s_add_u32 s49, s50, 0x10000
	s_addc_u32 s65, s51, 0
	s_mov_b32 s66, -2
	.p2align	6

.LBB0_1375:
	s_ashr_i32 s11, s10, 31
	s_lshl_b64 s[16:17], s[10:11], 22
	s_add_u32 s28, s12, s16
	s_addc_u32 s29, s13, s17
	s_and_b64 s[16:17], s[38:39], exec
	s_cselect_b32 s11, s29, s45
	s_cselect_b32 s56, s28, s44
	s_ashr_i32 s1, s0, 31
	s_lshl_b64 s[16:17], s[0:1], 22
	s_add_u32 s40, s20, s16
	s_addc_u32 s41, s21, s17
	s_and_b64 s[16:17], s[38:39], exec
	s_cselect_b32 s1, s41, s43
	s_cselect_b32 s57, s40, s42
	s_add_u32 s44, s44, 0xc000
	s_addc_u32 s45, s45, 0
	s_add_u32 s58, s42, 0x10000
	s_addc_u32 s59, s43, 0
	s_mov_b32 s60, -2
	.p2align	6
